# GELU epilogue 13 VALU per element: polynomial pre-scaled by 2^(1/16) so the 0.5 multiply folds into the final fma (same erf formula)
# speedup vs baseline: 1.1262x; 1.0025x over previous
_Z6gemm_kILi1ELi2ELi2EEvPKDF16_S1_iiiPKfS1_PDF16_PfS4_:
	s_lshr_b32 s37, s2, 3
	s_and_b32 s36, s2, 7
	s_lshr_b32 s38, s37, 3
	s_lshl_b32 s36, s36, 3
	s_add_u32 s22, s36, s38
	s_and_b32 s21, s37, 7
	s_cmp_ge_u32 s22, 63
	s_cbranch_scc1 Lg1_exit
	s_load_dwordx4 s[4:7], s[0:1], 0x0
	s_load_dwordx4 s[8:11], s[0:1], 0x20
	s_load_dwordx4 s[12:15], s[0:1], 0x30
	s_load_dwordx2 s[16:17], s[0:1], 0x40
	v_lshrrev_b32_e32 v20, 6, v0
	v_and_b32_e32 v1, 63, v0
	v_readfirstlane_b32 s20, v20
	v_and_b32_e32 v2, 15, v0
	v_bfe_u32 v3, v0, 4, 2
	v_and_b32_e32 v16, 7, v2
	v_xor_b32_e32 v16, v16, v3
	v_lshlrev_b32_e32 v16, 4, v16
	v_lshl_or_b32 v4, v2, 7, v16
	v_lshrrev_b32_e32 v16, 3, v1
	v_and_b32_e32 v17, 7, v1
	v_xor_b32_e32 v17, v17, v16
	v_lshlrev_b32_e32 v17, 4, v17
	v_lshl_or_b32 v9, v16, 7, v17
	v_add_u32_e32 v10, 0x140000, v9
	s_mul_i32 s23, s22, 10
	s_sub_u32 s24, 625, s23
	s_min_u32 s24, s24, 10
	s_waitcnt lgkmcnt(0)
	s_mul_i32 s36, s20, 0x280000
	s_lshl_b32 s37, s23, 11
	s_add_u32 s36, s36, s37
	s_add_u32 s26, s4, s36
	s_addc_u32 s27, s5, 0
	s_mul_i32 s28, s20, 0x1000
	s_add_u32 s46, s28, 0x10000
	s_mov_b32 s47, s28
	s_mov_b32 s29, 0
	s_lshl_b32 s36, s21, 7
	s_lshl_b32 s37, s20, 5
	s_add_u32 s36, s36, s37
	v_lshlrev_b32_e32 v16, 3, v3
	v_add_u32_e32 v16, s36, v16
	v_lshlrev_b32_e32 v17, 2, v16
	global_load_dwordx4 v[32:35], v17, s[8:9] offset:0
	global_load_dwordx4 v[36:39], v17, s[8:9] offset:16
	v_mov_b32_e32 v12, 0x36bc9e98
	s_mov_b32 s48, 0x3856241d
	s_mov_b32 s49, 0x382674aa
	s_mov_b32 s50, 0x3b605009
	s_mov_b32 s51, 0x3cb4dad2
	s_mov_b32 s52, 0x3d554cc4
	s_mov_b32 s53, 0x3f85aac3
	v_lshlrev_b32_e32 v18, 4, v3
	v_lshl_or_b32 v14, v2, 7, v18
	s_lshl_b32 s38, s21, 1
	s_lshr_b32 s39, s20, 1
	s_add_u32 s38, s38, s39
	s_mul_i32 s38, s38, 0x140000
	s_lshl_b32 s39, s23, 11
	s_add_u32 s38, s38, s39
	s_and_b32 s39, s20, 1
	s_lshl_b32 s39, s39, 6
	s_add_u32 s38, s38, s39
	s_add_u32 s30, s12, s38
	s_addc_u32 s31, s13, 0
	s_mov_b32 m0, s28
	s_add_u32 s28, s28, 0x4000
	s_cmp_ge_u32 s28, s46
	s_cselect_b32 s28, s47, s28
	global_load_lds_dwordx4 v9, s[26:27]
	global_load_lds_dwordx4 v9, s[26:27] offset:1024
	s_add_u32 m0, m0, 0x800
	s_nop 0
	global_load_lds_dwordx4 v10, s[26:27]
	global_load_lds_dwordx4 v10, s[26:27] offset:1024
	s_add_u32 s26, s26, 0x800
	s_addc_u32 s27, s27, 0
	s_mov_b32 m0, s28
	s_add_u32 s28, s28, 0x4000
	s_cmp_ge_u32 s28, s46
	s_cselect_b32 s28, s47, s28
	global_load_lds_dwordx4 v9, s[26:27]
	global_load_lds_dwordx4 v9, s[26:27] offset:1024
	s_add_u32 m0, m0, 0x800
	s_nop 0
	global_load_lds_dwordx4 v10, s[26:27]
	global_load_lds_dwordx4 v10, s[26:27] offset:1024
	s_add_u32 s26, s26, 0x800
	s_addc_u32 s27, s27, 0
	s_lshl_b32 s36, s21, 2
	s_add_u32 s36, s36, s20
	s_mul_i32 s36, s36, 0x8000
	v_lshlrev_b32_e32 v16, 4, v1
	v_add_u32_e32 v13, s36, v16
	global_load_dwordx4 a[0:3], v13, s[6:7] offset:0
	global_load_dwordx4 a[4:7], v13, s[6:7] offset:1024
	global_load_dwordx4 a[8:11], v13, s[6:7] offset:2048
	global_load_dwordx4 a[12:15], v13, s[6:7] offset:3072
	v_add_u32_e32 v13, 0x1000, v13
	global_load_dwordx4 a[16:19], v13, s[6:7] offset:0
	global_load_dwordx4 a[20:23], v13, s[6:7] offset:1024
	global_load_dwordx4 a[24:27], v13, s[6:7] offset:2048
	global_load_dwordx4 a[28:31], v13, s[6:7] offset:3072
	v_add_u32_e32 v13, 0x1000, v13
	global_load_dwordx4 a[32:35], v13, s[6:7] offset:0
	global_load_dwordx4 a[36:39], v13, s[6:7] offset:1024
	global_load_dwordx4 a[40:43], v13, s[6:7] offset:2048
	global_load_dwordx4 a[44:47], v13, s[6:7] offset:3072
	v_add_u32_e32 v13, 0x1000, v13
	global_load_dwordx4 a[48:51], v13, s[6:7] offset:0
	global_load_dwordx4 a[52:55], v13, s[6:7] offset:1024
	global_load_dwordx4 a[56:59], v13, s[6:7] offset:2048
	global_load_dwordx4 a[60:63], v13, s[6:7] offset:3072
	v_add_u32_e32 v13, 0x1000, v13
	global_load_dwordx4 a[64:67], v13, s[6:7] offset:0
	global_load_dwordx4 a[68:71], v13, s[6:7] offset:1024
	global_load_dwordx4 a[72:75], v13, s[6:7] offset:2048
	global_load_dwordx4 a[76:79], v13, s[6:7] offset:3072
	v_add_u32_e32 v13, 0x1000, v13
	global_load_dwordx4 a[80:83], v13, s[6:7] offset:0
	global_load_dwordx4 a[84:87], v13, s[6:7] offset:1024
	global_load_dwordx4 a[88:91], v13, s[6:7] offset:2048
	global_load_dwordx4 a[92:95], v13, s[6:7] offset:3072
	v_add_u32_e32 v13, 0x1000, v13
	global_load_dwordx4 a[96:99], v13, s[6:7] offset:0
	global_load_dwordx4 a[100:103], v13, s[6:7] offset:1024
	global_load_dwordx4 a[104:107], v13, s[6:7] offset:2048
	global_load_dwordx4 a[108:111], v13, s[6:7] offset:3072
	v_add_u32_e32 v13, 0x1000, v13
	global_load_dwordx4 a[112:115], v13, s[6:7] offset:0
	global_load_dwordx4 a[116:119], v13, s[6:7] offset:1024
	global_load_dwordx4 a[120:123], v13, s[6:7] offset:2048
	global_load_dwordx4 a[124:127], v13, s[6:7] offset:3072
	s_mov_b32 m0, s28
	s_add_u32 s28, s28, 0x4000
	s_cmp_ge_u32 s28, s46
	s_cselect_b32 s28, s47, s28
	global_load_lds_dwordx4 v9, s[26:27]
	global_load_lds_dwordx4 v9, s[26:27] offset:1024
	s_add_u32 m0, m0, 0x800
	s_nop 0
	global_load_lds_dwordx4 v10, s[26:27]
	global_load_lds_dwordx4 v10, s[26:27] offset:1024
	s_add_u32 s26, s26, 0x800
	s_addc_u32 s27, s27, 0
	s_waitcnt vmcnt(36)
	s_barrier
	v_add_u32_e32 v5, s29, v4
	v_xor_b32_e32 v6, 64, v5
	s_add_u32 s29, s29, 0x4000
	s_cmp_ge_u32 s29, 0x10000
	s_cselect_b32 s29, 0, s29
	ds_read_b128 v[64:67], v5 offset:0
	ds_read_b128 v[68:71], v6 offset:0
	ds_read_b128 v[72:75], v5 offset:2048
	ds_read_b128 v[76:79], v6 offset:2048
	ds_read_b128 v[80:83], v5 offset:4096
	ds_read_b128 v[84:87], v6 offset:4096
	ds_read_b128 v[88:91], v5 offset:6144
	ds_read_b128 v[92:95], v6 offset:6144
	ds_read_b128 v[96:99], v5 offset:8192
	ds_read_b128 v[100:103], v6 offset:8192
	ds_read_b128 v[104:107], v5 offset:10240
	ds_read_b128 v[108:111], v6 offset:10240
	ds_read_b128 v[112:115], v5 offset:12288
	ds_read_b128 v[116:119], v6 offset:12288
	ds_read_b128 v[120:123], v5 offset:14336
	ds_read_b128 v[124:127], v6 offset:14336
	v_add_u32_e32 v7, s29, v4
	v_xor_b32_e32 v8, 64, v7
	s_add_u32 s29, s29, 0x4000
	s_cmp_ge_u32 s29, 0x10000
	s_cselect_b32 s29, 0, s29
	s_mov_b32 m0, s28
	s_add_u32 s28, s28, 0x4000
	s_cmp_ge_u32 s28, s46
	s_cselect_b32 s28, s47, s28
	global_load_lds_dwordx4 v9, s[26:27]
	global_load_lds_dwordx4 v9, s[26:27] offset:1024
	s_add_u32 m0, m0, 0x800
	s_nop 0
	global_load_lds_dwordx4 v10, s[26:27]
	global_load_lds_dwordx4 v10, s[26:27] offset:1024
	s_add_u32 s26, s26, 0x800
	s_addc_u32 s27, s27, 0
	s_waitcnt vmcnt(38) lgkmcnt(15)
	v_mfma_f32_16x16x32_f16 v[40:43], a[0:3], v[64:67], v[32:35]
	v_mfma_f32_16x16x32_f16 v[44:47], a[4:7], v[64:67], v[36:39]
	ds_read_b128 v[64:67], v7 offset:0
	s_waitcnt vmcnt(36) lgkmcnt(15)
	v_mfma_f32_16x16x32_f16 v[40:43], a[8:11], v[68:71], v[40:43]
	v_mfma_f32_16x16x32_f16 v[44:47], a[12:15], v[68:71], v[44:47]
	ds_read_b128 v[68:71], v8 offset:0
	s_waitcnt vmcnt(34) lgkmcnt(15)
	v_mfma_f32_16x16x32_f16 v[40:43], a[16:19], v[72:75], v[40:43]
	v_mfma_f32_16x16x32_f16 v[44:47], a[20:23], v[72:75], v[44:47]
	ds_read_b128 v[72:75], v7 offset:2048
	s_waitcnt vmcnt(32) lgkmcnt(15)
	v_mfma_f32_16x16x32_f16 v[40:43], a[24:27], v[76:79], v[40:43]
	v_mfma_f32_16x16x32_f16 v[44:47], a[28:31], v[76:79], v[44:47]
	ds_read_b128 v[76:79], v8 offset:2048
	s_waitcnt vmcnt(30) lgkmcnt(15)
	v_mfma_f32_16x16x32_f16 v[40:43], a[32:35], v[80:83], v[40:43]
	v_mfma_f32_16x16x32_f16 v[44:47], a[36:39], v[80:83], v[44:47]
	ds_read_b128 v[80:83], v7 offset:4096
	s_waitcnt vmcnt(28) lgkmcnt(15)
	v_mfma_f32_16x16x32_f16 v[40:43], a[40:43], v[84:87], v[40:43]
	v_mfma_f32_16x16x32_f16 v[44:47], a[44:47], v[84:87], v[44:47]
	ds_read_b128 v[84:87], v8 offset:4096
	s_waitcnt vmcnt(26) lgkmcnt(15)
	v_mfma_f32_16x16x32_f16 v[40:43], a[48:51], v[88:91], v[40:43]
	v_mfma_f32_16x16x32_f16 v[44:47], a[52:55], v[88:91], v[44:47]
	ds_read_b128 v[88:91], v7 offset:6144
	s_waitcnt vmcnt(24) lgkmcnt(15)
	v_mfma_f32_16x16x32_f16 v[40:43], a[56:59], v[92:95], v[40:43]
	v_mfma_f32_16x16x32_f16 v[44:47], a[60:63], v[92:95], v[44:47]
	ds_read_b128 v[92:95], v8 offset:6144
	s_waitcnt vmcnt(22) lgkmcnt(15)
	v_mfma_f32_16x16x32_f16 v[40:43], a[64:67], v[96:99], v[40:43]
	v_mfma_f32_16x16x32_f16 v[44:47], a[68:71], v[96:99], v[44:47]
	ds_read_b128 v[96:99], v7 offset:8192
	s_waitcnt vmcnt(20) lgkmcnt(15)
	v_mfma_f32_16x16x32_f16 v[40:43], a[72:75], v[100:103], v[40:43]
	v_mfma_f32_16x16x32_f16 v[44:47], a[76:79], v[100:103], v[44:47]
	ds_read_b128 v[100:103], v8 offset:8192
	s_waitcnt vmcnt(18) lgkmcnt(15)
	v_mfma_f32_16x16x32_f16 v[40:43], a[80:83], v[104:107], v[40:43]
	v_mfma_f32_16x16x32_f16 v[44:47], a[84:87], v[104:107], v[44:47]
	ds_read_b128 v[104:107], v7 offset:10240
	s_waitcnt vmcnt(16) lgkmcnt(15)
	v_mfma_f32_16x16x32_f16 v[40:43], a[88:91], v[108:111], v[40:43]
	v_mfma_f32_16x16x32_f16 v[44:47], a[92:95], v[108:111], v[44:47]
	ds_read_b128 v[108:111], v8 offset:10240
	s_waitcnt vmcnt(14) lgkmcnt(15)
	v_mfma_f32_16x16x32_f16 v[40:43], a[96:99], v[112:115], v[40:43]
	v_mfma_f32_16x16x32_f16 v[44:47], a[100:103], v[112:115], v[44:47]
	ds_read_b128 v[112:115], v7 offset:12288
	s_waitcnt vmcnt(12) lgkmcnt(15)
	v_mfma_f32_16x16x32_f16 v[40:43], a[104:107], v[116:119], v[40:43]
	v_mfma_f32_16x16x32_f16 v[44:47], a[108:111], v[116:119], v[44:47]
	ds_read_b128 v[116:119], v8 offset:12288
	s_waitcnt vmcnt(10) lgkmcnt(15)
	v_mfma_f32_16x16x32_f16 v[40:43], a[112:115], v[120:123], v[40:43]
	v_mfma_f32_16x16x32_f16 v[44:47], a[116:119], v[120:123], v[44:47]
	ds_read_b128 v[120:123], v7 offset:14336
	s_waitcnt vmcnt(8) lgkmcnt(15)
	v_mfma_f32_16x16x32_f16 v[40:43], a[120:123], v[124:127], v[40:43]
	v_mfma_f32_16x16x32_f16 v[44:47], a[124:127], v[124:127], v[44:47]
	ds_read_b128 v[124:127], v8 offset:14336
Lg1_loop:
	s_waitcnt vmcnt(4)
	s_barrier
	v_add_u32_e32 v5, s29, v4
	v_xor_b32_e32 v6, 64, v5
	s_add_u32 s29, s29, 0x4000
	s_cmp_ge_u32 s29, 0x10000
	s_cselect_b32 s29, 0, s29
	s_waitcnt lgkmcnt(15)
	v_mfma_f32_16x16x32_f16 v[48:51], a[0:3], v[64:67], v[32:35]
	v_mfma_f32_16x16x32_f16 v[52:55], a[4:7], v[64:67], v[36:39]
	ds_read_b128 v[64:67], v5 offset:0
	v_fma_f32 v16, |v40|, v12, s48
	v_fma_f32 v16, |v40|, v16, s49
	v_fma_f32 v16, |v40|, v16, s50
	v_fma_f32 v16, |v40|, v16, s51
	s_waitcnt lgkmcnt(15)
	v_mfma_f32_16x16x32_f16 v[48:51], a[8:11], v[68:71], v[48:51]
	v_fma_f32 v16, |v40|, v16, s52
	v_fma_f32 v16, |v40|, v16, s53
	v_mul_f32_e32 v16, v16, v16
	v_mul_f32_e32 v16, v16, v16
	v_mfma_f32_16x16x32_f16 v[52:55], a[12:15], v[68:71], v[52:55]
	ds_read_b128 v[68:71], v6 offset:0
	v_mul_f32_e32 v16, v16, v16
	v_mul_f32_e32 v16, v16, v16
	v_rcp_f32_e32 v16, v16
	v_max_f32_e32 v17, 0, v40
	s_waitcnt lgkmcnt(15)
	v_mfma_f32_16x16x32_f16 v[48:51], a[16:19], v[72:75], v[48:51]
	v_fma_f32 v56, -|v40|, v16, v17
	v_fma_f32 v19, |v41|, v12, s48
	v_fma_f32 v19, |v41|, v19, s49
	v_fma_f32 v19, |v41|, v19, s50
	v_mfma_f32_16x16x32_f16 v[52:55], a[20:23], v[72:75], v[52:55]
	ds_read_b128 v[72:75], v5 offset:2048
	v_fma_f32 v19, |v41|, v19, s51
	v_fma_f32 v19, |v41|, v19, s52
	v_fma_f32 v19, |v41|, v19, s53
	v_mul_f32_e32 v19, v19, v19
	s_waitcnt lgkmcnt(15)
	v_mfma_f32_16x16x32_f16 v[48:51], a[24:27], v[76:79], v[48:51]
	v_mul_f32_e32 v19, v19, v19
	v_mul_f32_e32 v19, v19, v19
	v_mul_f32_e32 v19, v19, v19
	v_rcp_f32_e32 v19, v19
	v_mfma_f32_16x16x32_f16 v[52:55], a[28:31], v[76:79], v[52:55]
	ds_read_b128 v[76:79], v6 offset:2048
	v_max_f32_e32 v20, 0, v41
	v_fma_f32 v57, -|v41|, v19, v20
	v_fma_f32 v22, |v42|, v12, s48
	v_fma_f32 v22, |v42|, v22, s49
	s_waitcnt lgkmcnt(15)
	v_mfma_f32_16x16x32_f16 v[48:51], a[32:35], v[80:83], v[48:51]
	s_mov_b32 m0, s28
	s_add_u32 s28, s28, 0x4000
	s_cmp_ge_u32 s28, s46
	s_cselect_b32 s28, s47, s28
	global_load_lds_dwordx4 v9, s[26:27]
	v_fma_f32 v22, |v42|, v22, s50
	v_fma_f32 v22, |v42|, v22, s51
	v_fma_f32 v22, |v42|, v22, s52
	v_fma_f32 v22, |v42|, v22, s53
	v_mfma_f32_16x16x32_f16 v[52:55], a[36:39], v[80:83], v[52:55]
	ds_read_b128 v[80:83], v5 offset:4096
	v_mul_f32_e32 v22, v22, v22
	v_mul_f32_e32 v22, v22, v22
	v_mul_f32_e32 v22, v22, v22
	v_mul_f32_e32 v22, v22, v22
	s_waitcnt lgkmcnt(15)
	v_mfma_f32_16x16x32_f16 v[48:51], a[40:43], v[84:87], v[48:51]
	v_rcp_f32_e32 v22, v22
	v_max_f32_e32 v23, 0, v42
	v_fma_f32 v58, -|v42|, v22, v23
	v_mfma_f32_16x16x32_f16 v[52:55], a[44:47], v[84:87], v[52:55]
	ds_read_b128 v[84:87], v6 offset:4096
	v_fma_f32 v25, |v43|, v12, s48
	v_fma_f32 v25, |v43|, v25, s49
	v_fma_f32 v25, |v43|, v25, s50
	v_fma_f32 v25, |v43|, v25, s51
	s_waitcnt lgkmcnt(15)
	v_mfma_f32_16x16x32_f16 v[48:51], a[48:51], v[88:91], v[48:51]
	v_fma_f32 v25, |v43|, v25, s52
	v_fma_f32 v25, |v43|, v25, s53
	v_mul_f32_e32 v25, v25, v25
	v_mul_f32_e32 v25, v25, v25
	v_mfma_f32_16x16x32_f16 v[52:55], a[52:55], v[88:91], v[52:55]
	ds_read_b128 v[88:91], v5 offset:6144
	v_mul_f32_e32 v25, v25, v25
	v_mul_f32_e32 v25, v25, v25
	v_rcp_f32_e32 v25, v25
	v_max_f32_e32 v26, 0, v43
	s_waitcnt lgkmcnt(15)
	v_mfma_f32_16x16x32_f16 v[48:51], a[56:59], v[92:95], v[48:51]
	global_load_lds_dwordx4 v9, s[26:27] offset:1024
	v_fma_f32 v59, -|v43|, v25, v26
	v_fma_f32 v16, |v44|, v12, s48
	v_fma_f32 v16, |v44|, v16, s49
	v_fma_f32 v16, |v44|, v16, s50
	v_mfma_f32_16x16x32_f16 v[52:55], a[60:63], v[92:95], v[52:55]
	ds_read_b128 v[92:95], v6 offset:6144
	v_fma_f32 v16, |v44|, v16, s51
	v_fma_f32 v16, |v44|, v16, s52
	v_fma_f32 v16, |v44|, v16, s53
	v_mul_f32_e32 v16, v16, v16
	s_waitcnt lgkmcnt(15)
	v_mfma_f32_16x16x32_f16 v[48:51], a[64:67], v[96:99], v[48:51]
	v_mul_f32_e32 v16, v16, v16
	v_mul_f32_e32 v16, v16, v16
	v_mul_f32_e32 v16, v16, v16
	v_rcp_f32_e32 v16, v16
	v_mfma_f32_16x16x32_f16 v[52:55], a[68:71], v[96:99], v[52:55]
	ds_read_b128 v[96:99], v5 offset:8192
	v_max_f32_e32 v17, 0, v44
	v_fma_f32 v60, -|v44|, v16, v17
	v_fma_f32 v19, |v45|, v12, s48
	v_fma_f32 v19, |v45|, v19, s49
	s_waitcnt lgkmcnt(15)
	v_mfma_f32_16x16x32_f16 v[48:51], a[72:75], v[100:103], v[48:51]
	v_fma_f32 v19, |v45|, v19, s50
	v_fma_f32 v19, |v45|, v19, s51
	v_fma_f32 v19, |v45|, v19, s52
	v_fma_f32 v19, |v45|, v19, s53
	v_mfma_f32_16x16x32_f16 v[52:55], a[76:79], v[100:103], v[52:55]
	ds_read_b128 v[100:103], v6 offset:8192
	v_mul_f32_e32 v19, v19, v19
	v_mul_f32_e32 v19, v19, v19
	v_mul_f32_e32 v19, v19, v19
	s_waitcnt lgkmcnt(15)
	v_mfma_f32_16x16x32_f16 v[48:51], a[80:83], v[104:107], v[48:51]
	v_mul_f32_e32 v19, v19, v19
	v_rcp_f32_e32 v19, v19
	v_max_f32_e32 v20, 0, v45
	v_fma_f32 v61, -|v45|, v19, v20
	v_mfma_f32_16x16x32_f16 v[52:55], a[84:87], v[104:107], v[52:55]
	ds_read_b128 v[104:107], v5 offset:10240
	s_add_u32 m0, m0, 0x800
	s_nop 0
	global_load_lds_dwordx4 v10, s[26:27]
	v_fma_f32 v22, |v46|, v12, s48
	v_fma_f32 v22, |v46|, v22, s49
	v_fma_f32 v22, |v46|, v22, s50
	v_fma_f32 v22, |v46|, v22, s51
	s_waitcnt lgkmcnt(15)
	v_mfma_f32_16x16x32_f16 v[48:51], a[88:91], v[108:111], v[48:51]
	v_fma_f32 v22, |v46|, v22, s52
	v_fma_f32 v22, |v46|, v22, s53
	v_mul_f32_e32 v22, v22, v22
	v_mul_f32_e32 v22, v22, v22
	v_mfma_f32_16x16x32_f16 v[52:55], a[92:95], v[108:111], v[52:55]
	ds_read_b128 v[108:111], v6 offset:10240
	v_mul_f32_e32 v22, v22, v22
	v_mul_f32_e32 v22, v22, v22
	v_rcp_f32_e32 v22, v22
	v_max_f32_e32 v23, 0, v46
	s_waitcnt lgkmcnt(15)
	v_mfma_f32_16x16x32_f16 v[48:51], a[96:99], v[112:115], v[48:51]
	v_fma_f32 v62, -|v46|, v22, v23
	v_fma_f32 v25, |v47|, v12, s48
	v_fma_f32 v25, |v47|, v25, s49
	v_fma_f32 v25, |v47|, v25, s50
	v_mfma_f32_16x16x32_f16 v[52:55], a[100:103], v[112:115], v[52:55]
	ds_read_b128 v[112:115], v5 offset:12288
	v_fma_f32 v25, |v47|, v25, s51
	v_fma_f32 v25, |v47|, v25, s52
	v_fma_f32 v25, |v47|, v25, s53
	v_mul_f32_e32 v25, v25, v25
	s_waitcnt lgkmcnt(15)
	v_mfma_f32_16x16x32_f16 v[48:51], a[104:107], v[116:119], v[48:51]
	v_mul_f32_e32 v25, v25, v25
	v_mul_f32_e32 v25, v25, v25
	v_mul_f32_e32 v25, v25, v25
	v_rcp_f32_e32 v25, v25
	v_mfma_f32_16x16x32_f16 v[52:55], a[108:111], v[116:119], v[52:55]
	ds_read_b128 v[116:119], v6 offset:12288
	v_max_f32_e32 v26, 0, v47
	v_fma_f32 v63, -|v47|, v25, v26
	v_cvt_pk_f16_f32 v56, v56, v57
	v_cvt_pk_f16_f32 v57, v58, v59
	s_waitcnt lgkmcnt(15)
	v_mfma_f32_16x16x32_f16 v[48:51], a[112:115], v[120:123], v[48:51]
	global_load_lds_dwordx4 v10, s[26:27] offset:1024
	v_cvt_pk_f16_f32 v58, v60, v61
	v_cvt_pk_f16_f32 v59, v62, v63
	global_store_dwordx4 v14, v[56:59], s[30:31]
	v_mfma_f32_16x16x32_f16 v[52:55], a[116:119], v[120:123], v[52:55]
	ds_read_b128 v[120:123], v5 offset:14336
	s_add_u32 s26, s26, 0x800
	s_addc_u32 s27, s27, 0
	s_add_u32 s30, s30, 0x800
	s_addc_u32 s31, s31, 0
	s_waitcnt lgkmcnt(15)
	v_mfma_f32_16x16x32_f16 v[48:51], a[120:123], v[124:127], v[48:51]
	v_mfma_f32_16x16x32_f16 v[52:55], a[124:127], v[124:127], v[52:55]
	ds_read_b128 v[124:127], v6 offset:14336
	s_sub_u32 s24, s24, 1
	s_cmp_le_u32 s24, 1
	s_cbranch_scc1 Lg1_exitA
	s_waitcnt vmcnt(4)
	s_barrier
	v_add_u32_e32 v7, s29, v4
	v_xor_b32_e32 v8, 64, v7
	s_add_u32 s29, s29, 0x4000
	s_cmp_ge_u32 s29, 0x10000
	s_cselect_b32 s29, 0, s29
	s_waitcnt lgkmcnt(15)
	v_mfma_f32_16x16x32_f16 v[40:43], a[0:3], v[64:67], v[32:35]
	v_mfma_f32_16x16x32_f16 v[44:47], a[4:7], v[64:67], v[36:39]
	ds_read_b128 v[64:67], v7 offset:0
	v_fma_f32 v16, |v48|, v12, s48
	v_fma_f32 v16, |v48|, v16, s49
	v_fma_f32 v16, |v48|, v16, s50
	v_fma_f32 v16, |v48|, v16, s51
	s_waitcnt lgkmcnt(15)
	v_mfma_f32_16x16x32_f16 v[40:43], a[8:11], v[68:71], v[40:43]
	v_fma_f32 v16, |v48|, v16, s52
	v_fma_f32 v16, |v48|, v16, s53
	v_mul_f32_e32 v16, v16, v16
	v_mul_f32_e32 v16, v16, v16
	v_mfma_f32_16x16x32_f16 v[44:47], a[12:15], v[68:71], v[44:47]
	ds_read_b128 v[68:71], v8 offset:0
	v_mul_f32_e32 v16, v16, v16
	v_mul_f32_e32 v16, v16, v16
	v_rcp_f32_e32 v16, v16
	v_max_f32_e32 v17, 0, v48
	s_waitcnt lgkmcnt(15)
	v_mfma_f32_16x16x32_f16 v[40:43], a[16:19], v[72:75], v[40:43]
	v_fma_f32 v56, -|v48|, v16, v17
	v_fma_f32 v19, |v49|, v12, s48
	v_fma_f32 v19, |v49|, v19, s49
	v_fma_f32 v19, |v49|, v19, s50
	v_mfma_f32_16x16x32_f16 v[44:47], a[20:23], v[72:75], v[44:47]
	ds_read_b128 v[72:75], v7 offset:2048
	v_fma_f32 v19, |v49|, v19, s51
	v_fma_f32 v19, |v49|, v19, s52
	v_fma_f32 v19, |v49|, v19, s53
	v_mul_f32_e32 v19, v19, v19
	s_waitcnt lgkmcnt(15)
	v_mfma_f32_16x16x32_f16 v[40:43], a[24:27], v[76:79], v[40:43]
	v_mul_f32_e32 v19, v19, v19
	v_mul_f32_e32 v19, v19, v19
	v_mul_f32_e32 v19, v19, v19
	v_rcp_f32_e32 v19, v19
	v_mfma_f32_16x16x32_f16 v[44:47], a[28:31], v[76:79], v[44:47]
	ds_read_b128 v[76:79], v8 offset:2048
	v_max_f32_e32 v20, 0, v49
	v_fma_f32 v57, -|v49|, v19, v20
	v_fma_f32 v22, |v50|, v12, s48
	v_fma_f32 v22, |v50|, v22, s49
	s_waitcnt lgkmcnt(15)
	v_mfma_f32_16x16x32_f16 v[40:43], a[32:35], v[80:83], v[40:43]
	s_mov_b32 m0, s28
	s_add_u32 s28, s28, 0x4000
	s_cmp_ge_u32 s28, s46
	s_cselect_b32 s28, s47, s28
	global_load_lds_dwordx4 v9, s[26:27]
	v_fma_f32 v22, |v50|, v22, s50
	v_fma_f32 v22, |v50|, v22, s51
	v_fma_f32 v22, |v50|, v22, s52
	v_fma_f32 v22, |v50|, v22, s53
	v_mfma_f32_16x16x32_f16 v[44:47], a[36:39], v[80:83], v[44:47]
	ds_read_b128 v[80:83], v7 offset:4096
	v_mul_f32_e32 v22, v22, v22
	v_mul_f32_e32 v22, v22, v22
	v_mul_f32_e32 v22, v22, v22
	v_mul_f32_e32 v22, v22, v22
	s_waitcnt lgkmcnt(15)
	v_mfma_f32_16x16x32_f16 v[40:43], a[40:43], v[84:87], v[40:43]
	v_rcp_f32_e32 v22, v22
	v_max_f32_e32 v23, 0, v50
	v_fma_f32 v58, -|v50|, v22, v23
	v_mfma_f32_16x16x32_f16 v[44:47], a[44:47], v[84:87], v[44:47]
	ds_read_b128 v[84:87], v8 offset:4096
	v_fma_f32 v25, |v51|, v12, s48
	v_fma_f32 v25, |v51|, v25, s49
	v_fma_f32 v25, |v51|, v25, s50
	v_fma_f32 v25, |v51|, v25, s51
	s_waitcnt lgkmcnt(15)
	v_mfma_f32_16x16x32_f16 v[40:43], a[48:51], v[88:91], v[40:43]
	v_fma_f32 v25, |v51|, v25, s52
	v_fma_f32 v25, |v51|, v25, s53
	v_mul_f32_e32 v25, v25, v25
	v_mul_f32_e32 v25, v25, v25
	v_mfma_f32_16x16x32_f16 v[44:47], a[52:55], v[88:91], v[44:47]
	ds_read_b128 v[88:91], v7 offset:6144
	v_mul_f32_e32 v25, v25, v25
	v_mul_f32_e32 v25, v25, v25
	v_rcp_f32_e32 v25, v25
	v_max_f32_e32 v26, 0, v51
	s_waitcnt lgkmcnt(15)
	v_mfma_f32_16x16x32_f16 v[40:43], a[56:59], v[92:95], v[40:43]
	global_load_lds_dwordx4 v9, s[26:27] offset:1024
	v_fma_f32 v59, -|v51|, v25, v26
	v_fma_f32 v16, |v52|, v12, s48
	v_fma_f32 v16, |v52|, v16, s49
	v_fma_f32 v16, |v52|, v16, s50
	v_mfma_f32_16x16x32_f16 v[44:47], a[60:63], v[92:95], v[44:47]
	ds_read_b128 v[92:95], v8 offset:6144
	v_fma_f32 v16, |v52|, v16, s51
	v_fma_f32 v16, |v52|, v16, s52
	v_fma_f32 v16, |v52|, v16, s53
	v_mul_f32_e32 v16, v16, v16
	s_waitcnt lgkmcnt(15)
	v_mfma_f32_16x16x32_f16 v[40:43], a[64:67], v[96:99], v[40:43]
	v_mul_f32_e32 v16, v16, v16
	v_mul_f32_e32 v16, v16, v16
	v_mul_f32_e32 v16, v16, v16
	v_rcp_f32_e32 v16, v16
	v_mfma_f32_16x16x32_f16 v[44:47], a[68:71], v[96:99], v[44:47]
	ds_read_b128 v[96:99], v7 offset:8192
	v_max_f32_e32 v17, 0, v52
	v_fma_f32 v60, -|v52|, v16, v17
	v_fma_f32 v19, |v53|, v12, s48
	v_fma_f32 v19, |v53|, v19, s49
	s_waitcnt lgkmcnt(15)
	v_mfma_f32_16x16x32_f16 v[40:43], a[72:75], v[100:103], v[40:43]
	v_fma_f32 v19, |v53|, v19, s50
	v_fma_f32 v19, |v53|, v19, s51
	v_fma_f32 v19, |v53|, v19, s52
	v_fma_f32 v19, |v53|, v19, s53
	v_mfma_f32_16x16x32_f16 v[44:47], a[76:79], v[100:103], v[44:47]
	ds_read_b128 v[100:103], v8 offset:8192
	v_mul_f32_e32 v19, v19, v19
	v_mul_f32_e32 v19, v19, v19
	v_mul_f32_e32 v19, v19, v19
	s_waitcnt lgkmcnt(15)
	v_mfma_f32_16x16x32_f16 v[40:43], a[80:83], v[104:107], v[40:43]
	v_mul_f32_e32 v19, v19, v19
	v_rcp_f32_e32 v19, v19
	v_max_f32_e32 v20, 0, v53
	v_fma_f32 v61, -|v53|, v19, v20
	v_mfma_f32_16x16x32_f16 v[44:47], a[84:87], v[104:107], v[44:47]
	ds_read_b128 v[104:107], v7 offset:10240
	s_add_u32 m0, m0, 0x800
	s_nop 0
	global_load_lds_dwordx4 v10, s[26:27]
	v_fma_f32 v22, |v54|, v12, s48
	v_fma_f32 v22, |v54|, v22, s49
	v_fma_f32 v22, |v54|, v22, s50
	v_fma_f32 v22, |v54|, v22, s51
	s_waitcnt lgkmcnt(15)
	v_mfma_f32_16x16x32_f16 v[40:43], a[88:91], v[108:111], v[40:43]
	v_fma_f32 v22, |v54|, v22, s52
	v_fma_f32 v22, |v54|, v22, s53
	v_mul_f32_e32 v22, v22, v22
	v_mul_f32_e32 v22, v22, v22
	v_mfma_f32_16x16x32_f16 v[44:47], a[92:95], v[108:111], v[44:47]
	ds_read_b128 v[108:111], v8 offset:10240
	v_mul_f32_e32 v22, v22, v22
	v_mul_f32_e32 v22, v22, v22
	v_rcp_f32_e32 v22, v22
	v_max_f32_e32 v23, 0, v54
	s_waitcnt lgkmcnt(15)
	v_mfma_f32_16x16x32_f16 v[40:43], a[96:99], v[112:115], v[40:43]
	v_fma_f32 v62, -|v54|, v22, v23
	v_fma_f32 v25, |v55|, v12, s48
	v_fma_f32 v25, |v55|, v25, s49
	v_fma_f32 v25, |v55|, v25, s50
	v_mfma_f32_16x16x32_f16 v[44:47], a[100:103], v[112:115], v[44:47]
	ds_read_b128 v[112:115], v7 offset:12288
	v_fma_f32 v25, |v55|, v25, s51
	v_fma_f32 v25, |v55|, v25, s52
	v_fma_f32 v25, |v55|, v25, s53
	v_mul_f32_e32 v25, v25, v25
	s_waitcnt lgkmcnt(15)
	v_mfma_f32_16x16x32_f16 v[40:43], a[104:107], v[116:119], v[40:43]
	v_mul_f32_e32 v25, v25, v25
	v_mul_f32_e32 v25, v25, v25
	v_mul_f32_e32 v25, v25, v25
	v_rcp_f32_e32 v25, v25
	v_mfma_f32_16x16x32_f16 v[44:47], a[108:111], v[116:119], v[44:47]
	ds_read_b128 v[116:119], v8 offset:12288
	v_max_f32_e32 v26, 0, v55
	v_fma_f32 v63, -|v55|, v25, v26
	v_cvt_pk_f16_f32 v56, v56, v57
	v_cvt_pk_f16_f32 v57, v58, v59
	s_waitcnt lgkmcnt(15)
	v_mfma_f32_16x16x32_f16 v[40:43], a[112:115], v[120:123], v[40:43]
	global_load_lds_dwordx4 v10, s[26:27] offset:1024
	v_cvt_pk_f16_f32 v58, v60, v61
	v_cvt_pk_f16_f32 v59, v62, v63
	global_store_dwordx4 v14, v[56:59], s[30:31]
	v_mfma_f32_16x16x32_f16 v[44:47], a[116:119], v[120:123], v[44:47]
	ds_read_b128 v[120:123], v7 offset:14336
	s_add_u32 s26, s26, 0x800
	s_addc_u32 s27, s27, 0
	s_add_u32 s30, s30, 0x800
	s_addc_u32 s31, s31, 0
	s_waitcnt lgkmcnt(15)
	v_mfma_f32_16x16x32_f16 v[40:43], a[120:123], v[124:127], v[40:43]
	v_mfma_f32_16x16x32_f16 v[44:47], a[124:127], v[124:127], v[44:47]
	ds_read_b128 v[124:127], v8 offset:14336
	s_sub_u32 s24, s24, 1
	s_cmp_le_u32 s24, 1
	s_cbranch_scc0 Lg1_loop
	s_nop 7
	s_nop 7
	v_fma_f32 v16, |v40|, v12, s48
	v_fma_f32 v16, |v40|, v16, s49
	v_fma_f32 v16, |v40|, v16, s50
	v_fma_f32 v16, |v40|, v16, s51
	v_fma_f32 v16, |v40|, v16, s52
	v_fma_f32 v16, |v40|, v16, s53
	v_mul_f32_e32 v16, v16, v16
	v_mul_f32_e32 v16, v16, v16
	v_mul_f32_e32 v16, v16, v16
	v_mul_f32_e32 v16, v16, v16
	v_rcp_f32_e32 v16, v16
	v_max_f32_e32 v17, 0, v40
	v_fma_f32 v56, -|v40|, v16, v17
	v_fma_f32 v19, |v41|, v12, s48
	v_fma_f32 v19, |v41|, v19, s49
	v_fma_f32 v19, |v41|, v19, s50
	v_fma_f32 v19, |v41|, v19, s51
	v_fma_f32 v19, |v41|, v19, s52
	v_fma_f32 v19, |v41|, v19, s53
	v_mul_f32_e32 v19, v19, v19
	v_mul_f32_e32 v19, v19, v19
	v_mul_f32_e32 v19, v19, v19
	v_mul_f32_e32 v19, v19, v19
	v_rcp_f32_e32 v19, v19
	v_max_f32_e32 v20, 0, v41
	v_fma_f32 v57, -|v41|, v19, v20
	v_fma_f32 v22, |v42|, v12, s48
	v_fma_f32 v22, |v42|, v22, s49
	v_fma_f32 v22, |v42|, v22, s50
	v_fma_f32 v22, |v42|, v22, s51
	v_fma_f32 v22, |v42|, v22, s52
	v_fma_f32 v22, |v42|, v22, s53
	v_mul_f32_e32 v22, v22, v22
	v_mul_f32_e32 v22, v22, v22
	v_mul_f32_e32 v22, v22, v22
	v_mul_f32_e32 v22, v22, v22
	v_rcp_f32_e32 v22, v22
	v_max_f32_e32 v23, 0, v42
	v_fma_f32 v58, -|v42|, v22, v23
	v_fma_f32 v25, |v43|, v12, s48
	v_fma_f32 v25, |v43|, v25, s49
	v_fma_f32 v25, |v43|, v25, s50
	v_fma_f32 v25, |v43|, v25, s51
	v_fma_f32 v25, |v43|, v25, s52
	v_fma_f32 v25, |v43|, v25, s53
	v_mul_f32_e32 v25, v25, v25
	v_mul_f32_e32 v25, v25, v25
	v_mul_f32_e32 v25, v25, v25
	v_mul_f32_e32 v25, v25, v25
	v_rcp_f32_e32 v25, v25
	v_max_f32_e32 v26, 0, v43
	v_fma_f32 v59, -|v43|, v25, v26
	v_fma_f32 v16, |v44|, v12, s48
	v_fma_f32 v16, |v44|, v16, s49
	v_fma_f32 v16, |v44|, v16, s50
	v_fma_f32 v16, |v44|, v16, s51
	v_fma_f32 v16, |v44|, v16, s52
	v_fma_f32 v16, |v44|, v16, s53
	v_mul_f32_e32 v16, v16, v16
	v_mul_f32_e32 v16, v16, v16
	v_mul_f32_e32 v16, v16, v16
	v_mul_f32_e32 v16, v16, v16
	v_rcp_f32_e32 v16, v16
	v_max_f32_e32 v17, 0, v44
	v_fma_f32 v60, -|v44|, v16, v17
	v_fma_f32 v19, |v45|, v12, s48
	v_fma_f32 v19, |v45|, v19, s49
	v_fma_f32 v19, |v45|, v19, s50
	v_fma_f32 v19, |v45|, v19, s51
	v_fma_f32 v19, |v45|, v19, s52
	v_fma_f32 v19, |v45|, v19, s53
	v_mul_f32_e32 v19, v19, v19
	v_mul_f32_e32 v19, v19, v19
	v_mul_f32_e32 v19, v19, v19
	v_mul_f32_e32 v19, v19, v19
	v_rcp_f32_e32 v19, v19
	v_max_f32_e32 v20, 0, v45
	v_fma_f32 v61, -|v45|, v19, v20
	v_fma_f32 v22, |v46|, v12, s48
	v_fma_f32 v22, |v46|, v22, s49
	v_fma_f32 v22, |v46|, v22, s50
	v_fma_f32 v22, |v46|, v22, s51
	v_fma_f32 v22, |v46|, v22, s52
	v_fma_f32 v22, |v46|, v22, s53
	v_mul_f32_e32 v22, v22, v22
	v_mul_f32_e32 v22, v22, v22
	v_mul_f32_e32 v22, v22, v22
	v_mul_f32_e32 v22, v22, v22
	v_rcp_f32_e32 v22, v22
	v_max_f32_e32 v23, 0, v46
	v_fma_f32 v62, -|v46|, v22, v23
	v_fma_f32 v25, |v47|, v12, s48
	v_fma_f32 v25, |v47|, v25, s49
	v_fma_f32 v25, |v47|, v25, s50
	v_fma_f32 v25, |v47|, v25, s51
	v_fma_f32 v25, |v47|, v25, s52
	v_fma_f32 v25, |v47|, v25, s53
	v_mul_f32_e32 v25, v25, v25
	v_mul_f32_e32 v25, v25, v25
	v_mul_f32_e32 v25, v25, v25
	v_mul_f32_e32 v25, v25, v25
	v_rcp_f32_e32 v25, v25
	v_max_f32_e32 v26, 0, v47
	v_fma_f32 v63, -|v47|, v25, v26
	v_cvt_pk_f16_f32 v56, v56, v57
	v_cvt_pk_f16_f32 v57, v58, v59
	v_cvt_pk_f16_f32 v58, v60, v61
	v_cvt_pk_f16_f32 v59, v62, v63
	global_store_dwordx4 v14, v[56:59], s[30:31]
	s_add_u32 s30, s30, 0x800
	s_addc_u32 s31, s31, 0
	s_endpgm
Lg1_exitA:
	s_nop 7
	s_nop 7
	v_fma_f32 v16, |v48|, v12, s48
	v_fma_f32 v16, |v48|, v16, s49
	v_fma_f32 v16, |v48|, v16, s50
	v_fma_f32 v16, |v48|, v16, s51
	v_fma_f32 v16, |v48|, v16, s52
	v_fma_f32 v16, |v48|, v16, s53
	v_mul_f32_e32 v16, v16, v16
	v_mul_f32_e32 v16, v16, v16
	v_mul_f32_e32 v16, v16, v16
	v_mul_f32_e32 v16, v16, v16
	v_rcp_f32_e32 v16, v16
	v_max_f32_e32 v17, 0, v48
	v_fma_f32 v56, -|v48|, v16, v17
	v_fma_f32 v19, |v49|, v12, s48
	v_fma_f32 v19, |v49|, v19, s49
	v_fma_f32 v19, |v49|, v19, s50
	v_fma_f32 v19, |v49|, v19, s51
	v_fma_f32 v19, |v49|, v19, s52
	v_fma_f32 v19, |v49|, v19, s53
	v_mul_f32_e32 v19, v19, v19
	v_mul_f32_e32 v19, v19, v19
	v_mul_f32_e32 v19, v19, v19
	v_mul_f32_e32 v19, v19, v19
	v_rcp_f32_e32 v19, v19
	v_max_f32_e32 v20, 0, v49
	v_fma_f32 v57, -|v49|, v19, v20
	v_fma_f32 v22, |v50|, v12, s48
	v_fma_f32 v22, |v50|, v22, s49
	v_fma_f32 v22, |v50|, v22, s50
	v_fma_f32 v22, |v50|, v22, s51
	v_fma_f32 v22, |v50|, v22, s52
	v_fma_f32 v22, |v50|, v22, s53
	v_mul_f32_e32 v22, v22, v22
	v_mul_f32_e32 v22, v22, v22
	v_mul_f32_e32 v22, v22, v22
	v_mul_f32_e32 v22, v22, v22
	v_rcp_f32_e32 v22, v22
	v_max_f32_e32 v23, 0, v50
	v_fma_f32 v58, -|v50|, v22, v23
	v_fma_f32 v25, |v51|, v12, s48
	v_fma_f32 v25, |v51|, v25, s49
	v_fma_f32 v25, |v51|, v25, s50
	v_fma_f32 v25, |v51|, v25, s51
	v_fma_f32 v25, |v51|, v25, s52
	v_fma_f32 v25, |v51|, v25, s53
	v_mul_f32_e32 v25, v25, v25
	v_mul_f32_e32 v25, v25, v25
	v_mul_f32_e32 v25, v25, v25
	v_mul_f32_e32 v25, v25, v25
	v_rcp_f32_e32 v25, v25
	v_max_f32_e32 v26, 0, v51
	v_fma_f32 v59, -|v51|, v25, v26
	v_fma_f32 v16, |v52|, v12, s48
	v_fma_f32 v16, |v52|, v16, s49
	v_fma_f32 v16, |v52|, v16, s50
	v_fma_f32 v16, |v52|, v16, s51
	v_fma_f32 v16, |v52|, v16, s52
	v_fma_f32 v16, |v52|, v16, s53
	v_mul_f32_e32 v16, v16, v16
	v_mul_f32_e32 v16, v16, v16
	v_mul_f32_e32 v16, v16, v16
	v_mul_f32_e32 v16, v16, v16
	v_rcp_f32_e32 v16, v16
	v_max_f32_e32 v17, 0, v52
	v_fma_f32 v60, -|v52|, v16, v17
	v_fma_f32 v19, |v53|, v12, s48
	v_fma_f32 v19, |v53|, v19, s49
	v_fma_f32 v19, |v53|, v19, s50
	v_fma_f32 v19, |v53|, v19, s51
	v_fma_f32 v19, |v53|, v19, s52
	v_fma_f32 v19, |v53|, v19, s53
	v_mul_f32_e32 v19, v19, v19
	v_mul_f32_e32 v19, v19, v19
	v_mul_f32_e32 v19, v19, v19
	v_mul_f32_e32 v19, v19, v19
	v_rcp_f32_e32 v19, v19
	v_max_f32_e32 v20, 0, v53
	v_fma_f32 v61, -|v53|, v19, v20
	v_fma_f32 v22, |v54|, v12, s48
	v_fma_f32 v22, |v54|, v22, s49
	v_fma_f32 v22, |v54|, v22, s50
	v_fma_f32 v22, |v54|, v22, s51
	v_fma_f32 v22, |v54|, v22, s52
	v_fma_f32 v22, |v54|, v22, s53
	v_mul_f32_e32 v22, v22, v22
	v_mul_f32_e32 v22, v22, v22
	v_mul_f32_e32 v22, v22, v22
	v_mul_f32_e32 v22, v22, v22
	v_rcp_f32_e32 v22, v22
	v_max_f32_e32 v23, 0, v54
	v_fma_f32 v62, -|v54|, v22, v23
	v_fma_f32 v25, |v55|, v12, s48
	v_fma_f32 v25, |v55|, v25, s49
	v_fma_f32 v25, |v55|, v25, s50
	v_fma_f32 v25, |v55|, v25, s51
	v_fma_f32 v25, |v55|, v25, s52
	v_fma_f32 v25, |v55|, v25, s53
	v_mul_f32_e32 v25, v25, v25
	v_mul_f32_e32 v25, v25, v25
	v_mul_f32_e32 v25, v25, v25
	v_mul_f32_e32 v25, v25, v25
	v_rcp_f32_e32 v25, v25
	v_max_f32_e32 v26, 0, v55
	v_fma_f32 v63, -|v55|, v25, v26
	v_cvt_pk_f16_f32 v56, v56, v57
	v_cvt_pk_f16_f32 v57, v58, v59
	v_cvt_pk_f16_f32 v58, v60, v61
	v_cvt_pk_f16_f32 v59, v62, v63
	global_store_dwordx4 v14, v[56:59], s[30:31]
	s_add_u32 s30, s30, 0x800
	s_addc_u32 s31, s31, 0
	s_endpgm
